# best version plus static s_setprio 2 for the four compute waves
# speedup vs baseline: 1.0022x; 1.0022x over previous
_Z11main_kernelPKfS0_PKDF16_S0_PfS3_:
	s_load_dwordx4 s[16:19], s[0:1], 0x0
	s_load_dwordx2 s[14:15], s[0:1], 0x28
	v_readfirstlane_b32 s3, v0
	v_and_b32_e32 v164, 63, v0
	s_ashr_i32 s33, s3, 6
	v_lshlrev_b32_e32 v162, 4, v164
	s_cmp_lg_u32 s33, 4
	s_mov_b64 s[4:5], -1
	s_cbranch_scc0 .LBB1_183
	s_load_dwordx2 s[20:21], s[0:1], 0x20
	s_lshl_b32 s98, s2, 7
	s_add_i32 s23, s33, -5
	s_cmp_gt_u32 s23, 1
	s_cbranch_scc0 .LBB1_142
	s_cmp_lg_u32 s33, 7
	v_writelane_b32 v216, s23, 0
	s_cbranch_scc0 .LBB1_95
	s_setprio 2
	s_lshl_b32 s3, s33, 5
	s_add_i32 s10, s3, s98
	s_or_b32 s4, s10, 1
	s_ashr_i32 s5, s4, 31
	s_lshl_b64 s[8:9], s[4:5], 10
	s_or_b32 s4, s10, 2
	s_ashr_i32 s5, s4, 31
	s_lshl_b64 s[12:13], s[4:5], 10
	s_or_b32 s4, s10, 3
	s_ashr_i32 s5, s4, 31
	s_lshl_b64 s[22:23], s[4:5], 10
	s_or_b32 s4, s10, 4
	s_ashr_i32 s5, s4, 31
	s_lshl_b64 s[24:25], s[4:5], 10
	s_or_b32 s4, s10, 5
	s_ashr_i32 s5, s4, 31
	s_lshl_b64 s[28:29], s[4:5], 10
	s_or_b32 s4, s10, 6
	s_ashr_i32 s5, s4, 31
	s_lshl_b64 s[26:27], s[4:5], 10
	s_or_b32 s4, s10, 7
	s_ashr_i32 s5, s4, 31
	s_lshl_b64 s[30:31], s[4:5], 10
	s_or_b32 s4, s10, 8
	s_ashr_i32 s5, s4, 31
	s_lshl_b64 s[34:35], s[4:5], 10
	s_or_b32 s4, s10, 9
	s_ashr_i32 s5, s4, 31
	s_lshl_b64 s[38:39], s[4:5], 10
	s_or_b32 s4, s10, 10
	s_ashr_i32 s5, s4, 31
	s_lshl_b64 s[36:37], s[4:5], 10
	s_or_b32 s4, s10, 11
	s_ashr_i32 s5, s4, 31
	s_lshl_b64 s[40:41], s[4:5], 10
	s_or_b32 s4, s10, 12
	s_ashr_i32 s5, s4, 31
	s_lshl_b64 s[42:43], s[4:5], 10
	s_or_b32 s4, s10, 13
	s_ashr_i32 s5, s4, 31
	s_lshl_b64 s[46:47], s[4:5], 10
	s_or_b32 s4, s10, 14
	v_mov_b32_e32 v163, 0
	s_ashr_i32 s11, s10, 31
	s_ashr_i32 s5, s4, 31
	s_waitcnt lgkmcnt(0)
	v_lshl_add_u64 v[166:167], s[16:17], 0, v[162:163]
	s_lshl_b64 s[6:7], s[10:11], 10
	s_lshl_b64 s[44:45], s[4:5], 10
	s_mul_i32 s4, s33, 0x4200
	v_lshl_add_u64 v[2:3], v[166:167], 0, s[6:7]
	v_mov_b32_e32 v1, s4
	v_lshl_or_b32 v78, v164, 3, s4
	s_or_b32 s4, s10, 15
	v_lshl_add_u64 v[4:5], v[166:167], 0, s[8:9]
	global_load_dwordx4 v[6:9], v[2:3], off nt
	global_load_dwordx4 v[10:13], v[4:5], off nt
	s_ashr_i32 s5, s4, 31
	v_lshl_add_u64 v[2:3], v[166:167], 0, s[12:13]
	s_lshl_b64 s[4:5], s[4:5], 10
	v_lshl_add_u64 v[4:5], v[166:167], 0, s[22:23]
	global_load_dwordx4 v[14:17], v[2:3], off nt
	global_load_dwordx4 v[18:21], v[4:5], off nt
	v_lshl_add_u64 v[2:3], v[166:167], 0, s[24:25]
	v_lshl_add_u64 v[66:67], v[166:167], 0, s[4:5]
	global_load_dwordx4 v[22:25], v[2:3], off nt
	v_add_u32_e32 v79, 0x1800, v78
	global_load_dwordx4 v[66:69], v[66:67], off nt
	v_lshl_add_u64 v[2:3], v[166:167], 0, s[28:29]
	global_load_dwordx4 v[26:29], v[2:3], off nt
	v_lshl_add_u64 v[2:3], v[166:167], 0, s[26:27]
	global_load_dwordx4 v[30:33], v[2:3], off nt
	v_lshl_add_u64 v[2:3], v[166:167], 0, s[30:31]
	global_load_dwordx4 v[34:37], v[2:3], off nt
	v_lshl_add_u64 v[2:3], v[166:167], 0, s[34:35]
	global_load_dwordx4 v[38:41], v[2:3], off nt
	v_lshl_add_u64 v[2:3], v[166:167], 0, s[38:39]
	global_load_dwordx4 v[42:45], v[2:3], off nt
	v_lshl_add_u64 v[2:3], v[166:167], 0, s[36:37]
	global_load_dwordx4 v[46:49], v[2:3], off nt
	v_lshl_add_u64 v[2:3], v[166:167], 0, s[40:41]
	global_load_dwordx4 v[50:53], v[2:3], off nt
	v_lshl_add_u64 v[2:3], v[166:167], 0, s[42:43]
	global_load_dwordx4 v[54:57], v[2:3], off nt
	v_lshl_add_u64 v[2:3], v[166:167], 0, s[46:47]
	global_load_dwordx4 v[58:61], v[2:3], off nt
	v_lshl_add_u64 v[2:3], v[166:167], 0, s[44:45]
	global_load_dwordx4 v[62:65], v[2:3], off nt
	v_lshl_add_u64 v[2:3], s[20:21], 0, v[162:163]
	v_lshl_add_u64 v[70:71], v[2:3], 0, s[6:7]
	s_or_b32 s6, s10, 16
	s_ashr_i32 s7, s6, 31
	s_lshl_b64 s[6:7], s[6:7], 10
	s_or_b32 s48, s10, 31
	s_ashr_i32 s49, s48, 31
	s_lshl_b64 s[48:49], s[48:49], 10
	v_lshl_add_u64 v[74:75], v[166:167], 0, s[48:49]
	v_and_b32_e32 v4, 31, v0
	v_lshrrev_b32_e32 v5, 5, v164
	v_add_u32_e32 v182, s10, v164
	v_mov_b32_e32 v179, 0x260
	v_add_u32_e32 v185, s3, v164
	v_mov_b32_e32 v177, 0xfffffe00
	v_or_b32_e32 v181, 0x10800, v162
	v_lshlrev_b32_e32 v184, 2, v5
	v_lshl_or_b32 v189, s33, 13, v164
	v_mov_b32_e32 v190, 0x22630
	v_mov_b32_e32 v191, 0x22634
	v_mov_b32_e32 v192, 0x22610
	v_mov_b32_e32 v193, 0x22600
	s_mov_b32 s50, 0x22624
	v_mov_b32_e32 v194, 0x22400
	v_mov_b32_e32 v170, 0x8800759c
	v_mov_b32_e32 v171, 0x7e37e43c
	s_waitcnt vmcnt(15)
	global_store_dwordx4 v[70:71], v[6:9], off nt
	s_nop 1
	v_cvt_pk_f16_f32 v9, v8, v9
	v_cvt_pk_f16_f32 v8, v6, v7
	v_lshl_add_u64 v[6:7], v[2:3], 0, s[8:9]
	s_waitcnt vmcnt(15)
	global_store_dwordx4 v[6:7], v[10:13], off nt
	v_cvt_pk_f16_f32 v7, v12, v13
	v_cvt_pk_f16_f32 v6, v10, v11
	ds_write2_b64 v78, v[8:9], v[6:7] offset1:66
	v_lshl_add_u64 v[6:7], v[2:3], 0, s[12:13]
	v_lshl_add_u64 v[8:9], v[2:3], 0, s[22:23]
	s_waitcnt vmcnt(15)
	global_store_dwordx4 v[6:7], v[14:17], off nt
	v_cvt_pk_f16_f32 v7, v16, v17
	v_cvt_pk_f16_f32 v6, v14, v15
	s_waitcnt vmcnt(15)
	global_store_dwordx4 v[8:9], v[18:21], off nt
	v_cvt_pk_f16_f32 v9, v20, v21
	v_cvt_pk_f16_f32 v8, v18, v19
	ds_write2_b64 v78, v[6:7], v[8:9] offset0:132 offset1:198
	v_lshl_add_u64 v[6:7], v[2:3], 0, s[24:25]
	v_lshl_add_u64 v[8:9], v[2:3], 0, s[28:29]
	s_waitcnt vmcnt(15)
	global_store_dwordx4 v[6:7], v[22:25], off nt
	v_cvt_pk_f16_f32 v7, v24, v25
	v_cvt_pk_f16_f32 v6, v22, v23
	s_waitcnt vmcnt(14)
	global_store_dwordx4 v[8:9], v[26:29], off nt
	v_cvt_pk_f16_f32 v9, v28, v29
	v_cvt_pk_f16_f32 v8, v26, v27
	v_add_u32_e32 v10, 0x800, v78
	ds_write2_b64 v10, v[6:7], v[8:9] offset0:8 offset1:74
	v_lshl_add_u64 v[6:7], v[2:3], 0, s[26:27]
	v_lshl_add_u64 v[8:9], v[2:3], 0, s[30:31]
	s_waitcnt vmcnt(14)
	global_store_dwordx4 v[6:7], v[30:33], off nt
	v_cvt_pk_f16_f32 v7, v32, v33
	v_cvt_pk_f16_f32 v6, v30, v31
	s_waitcnt vmcnt(14)
	global_store_dwordx4 v[8:9], v[34:37], off nt
	v_cvt_pk_f16_f32 v9, v36, v37
	v_cvt_pk_f16_f32 v8, v34, v35
	ds_write2_b64 v10, v[6:7], v[8:9] offset0:140 offset1:206
	v_lshl_add_u64 v[6:7], v[2:3], 0, s[34:35]
	v_lshl_add_u64 v[8:9], v[2:3], 0, s[38:39]
	s_waitcnt vmcnt(14)
	global_store_dwordx4 v[6:7], v[38:41], off nt
	v_cvt_pk_f16_f32 v7, v40, v41
	v_cvt_pk_f16_f32 v6, v38, v39
	s_waitcnt vmcnt(14)
	global_store_dwordx4 v[8:9], v[42:45], off nt
	v_cvt_pk_f16_f32 v9, v44, v45
	v_cvt_pk_f16_f32 v8, v42, v43
	v_add_u32_e32 v10, 0x1000, v78
	ds_write2_b64 v10, v[6:7], v[8:9] offset0:16 offset1:82
	v_lshl_add_u64 v[6:7], v[2:3], 0, s[36:37]
	v_lshl_add_u64 v[8:9], v[2:3], 0, s[40:41]
	s_waitcnt vmcnt(14)
	global_store_dwordx4 v[6:7], v[46:49], off nt
	v_cvt_pk_f16_f32 v7, v48, v49
	v_cvt_pk_f16_f32 v6, v46, v47
	s_waitcnt vmcnt(14)
	global_store_dwordx4 v[8:9], v[50:53], off nt
	v_cvt_pk_f16_f32 v9, v52, v53
	v_cvt_pk_f16_f32 v8, v50, v51
	ds_write2_b64 v10, v[6:7], v[8:9] offset0:148 offset1:214
	v_lshl_add_u64 v[6:7], v[2:3], 0, s[42:43]
	v_lshl_add_u64 v[8:9], v[2:3], 0, s[46:47]
	s_waitcnt vmcnt(14)
	global_store_dwordx4 v[6:7], v[54:57], off nt
	v_cvt_pk_f16_f32 v7, v56, v57
	v_cvt_pk_f16_f32 v6, v54, v55
	s_waitcnt vmcnt(14)
	global_store_dwordx4 v[8:9], v[58:61], off nt
	v_cvt_pk_f16_f32 v9, v60, v61
	v_cvt_pk_f16_f32 v8, v58, v59
	s_or_b32 s8, s10, 17
	ds_write2_b64 v79, v[6:7], v[8:9] offset0:24 offset1:90
	v_lshl_add_u64 v[6:7], v[2:3], 0, s[44:45]
	s_ashr_i32 s9, s8, 31
	s_or_b32 s12, s10, 18
	s_waitcnt vmcnt(14)
	global_store_dwordx4 v[6:7], v[62:65], off nt
	v_lshl_add_u64 v[14:15], v[166:167], 0, s[6:7]
	s_lshl_b64 s[8:9], s[8:9], 10
	s_ashr_i32 s13, s12, 31
	s_or_b32 s22, s10, 19
	v_lshl_add_u64 v[16:17], v[166:167], 0, s[8:9]
	global_load_dwordx4 v[6:9], v[14:15], off nt
	global_load_dwordx4 v[10:13], v[16:17], off nt
	s_lshl_b64 s[12:13], s[12:13], 10
	s_ashr_i32 s23, s22, 31
	s_or_b32 s24, s10, 20
	s_or_b32 s26, s10, 21
	v_lshl_add_u64 v[22:23], v[166:167], 0, s[12:13]
	s_lshl_b64 s[22:23], s[22:23], 10
	s_ashr_i32 s25, s24, 31
	s_ashr_i32 s27, s26, 31
	v_lshl_add_u64 v[24:25], v[166:167], 0, s[22:23]
	global_load_dwordx4 v[14:17], v[22:23], off nt
	global_load_dwordx4 v[18:21], v[24:25], off nt
	s_lshl_b64 s[24:25], s[24:25], 10
	s_lshl_b64 s[28:29], s[26:27], 10
	s_or_b32 s26, s10, 22
	s_or_b32 s30, s10, 23
	v_lshl_add_u64 v[22:23], v[166:167], 0, s[24:25]
	v_lshl_add_u64 v[26:27], v[166:167], 0, s[28:29]
	s_ashr_i32 s27, s26, 31
	s_ashr_i32 s31, s30, 31
	global_load_dwordx4 v[22:25], v[22:23], off nt
	s_lshl_b64 s[26:27], s[26:27], 10
	global_load_dwordx4 v[26:29], v[26:27], off nt
	s_lshl_b64 s[30:31], s[30:31], 10
	s_or_b32 s34, s10, 24
	s_or_b32 s36, s10, 25
	v_lshl_add_u64 v[30:31], v[166:167], 0, s[26:27]
	v_lshl_add_u64 v[34:35], v[166:167], 0, s[30:31]
	s_ashr_i32 s35, s34, 31
	s_ashr_i32 s37, s36, 31
	global_load_dwordx4 v[30:33], v[30:31], off nt
	s_lshl_b64 s[34:35], s[34:35], 10
	global_load_dwordx4 v[34:37], v[34:35], off nt
	s_lshl_b64 s[38:39], s[36:37], 10
	s_or_b32 s36, s10, 26
	s_or_b32 s40, s10, 27
	v_lshl_add_u64 v[38:39], v[166:167], 0, s[34:35]
	v_lshl_add_u64 v[42:43], v[166:167], 0, s[38:39]
	s_ashr_i32 s37, s36, 31
	s_ashr_i32 s41, s40, 31
	global_load_dwordx4 v[38:41], v[38:39], off nt
	s_lshl_b64 s[36:37], s[36:37], 10
	global_load_dwordx4 v[42:45], v[42:43], off nt
	s_lshl_b64 s[40:41], s[40:41], 10
	s_or_b32 s42, s10, 28
	s_or_b32 s44, s10, 29
	v_lshl_add_u64 v[46:47], v[166:167], 0, s[36:37]
	v_lshl_add_u64 v[50:51], v[166:167], 0, s[40:41]
	s_ashr_i32 s43, s42, 31
	s_ashr_i32 s45, s44, 31
	global_load_dwordx4 v[46:49], v[46:47], off nt
	s_lshl_b64 s[42:43], s[42:43], 10
	global_load_dwordx4 v[50:53], v[50:51], off nt
	s_lshl_b64 s[46:47], s[44:45], 10
	s_or_b32 s44, s10, 30
	v_lshl_add_u64 v[54:55], v[166:167], 0, s[42:43]
	v_lshl_add_u64 v[58:59], v[166:167], 0, s[46:47]
	s_ashr_i32 s45, s44, 31
	global_load_dwordx4 v[54:57], v[54:55], off nt
	s_lshl_b64 s[44:45], s[44:45], 10
	global_load_dwordx4 v[58:61], v[58:59], off nt
	v_lshl_add_u64 v[70:71], v[166:167], 0, s[44:45]
	global_load_dwordx4 v[70:73], v[70:71], off nt
	v_cvt_pk_f16_f32 v65, v64, v65
	global_load_dwordx4 v[74:77], v[74:75], off nt
	v_cvt_pk_f16_f32 v64, v62, v63
	v_lshl_add_u64 v[62:63], v[2:3], 0, s[4:5]
	global_store_dwordx4 v[62:63], v[66:69], off nt
	v_cvt_pk_f16_f32 v63, v68, v69
	v_cvt_pk_f16_f32 v62, v66, v67
	ds_write2_b64 v79, v[64:65], v[62:63] offset0:156 offset1:222
	v_lshl_add_u64 v[62:63], v[2:3], 0, s[6:7]
	s_movk_i32 s4, 0x210
	v_mad_u32_u24 v1, v4, s4, v1
	s_add_i32 s10, s10, 0x18000
	s_ashr_i32 s11, s10, 31
	v_add_u32_e32 v187, s10, v164
	s_lshl_b64 s[10:11], s[10:11], 10
	v_cmp_eq_u32_e64 s[6:7], 0, v164
	s_waitcnt vmcnt(16)
	global_store_dwordx4 v[62:63], v[6:9], off nt
	s_nop 1
	v_cvt_pk_f16_f32 v9, v8, v9
	v_cvt_pk_f16_f32 v8, v6, v7
	v_lshl_add_u64 v[6:7], v[2:3], 0, s[8:9]
	s_waitcnt vmcnt(16)
	global_store_dwordx4 v[6:7], v[10:13], off nt
	v_cvt_pk_f16_f32 v7, v12, v13
	v_cvt_pk_f16_f32 v6, v10, v11
	v_add_u32_e32 v10, 0x2000, v78
	ds_write2_b64 v10, v[8:9], v[6:7] offset0:32 offset1:98
	v_lshl_add_u64 v[6:7], v[2:3], 0, s[12:13]
	v_lshl_add_u64 v[8:9], v[2:3], 0, s[22:23]
	s_waitcnt vmcnt(16)
	global_store_dwordx4 v[6:7], v[14:17], off nt
	v_cvt_pk_f16_f32 v7, v16, v17
	v_cvt_pk_f16_f32 v6, v14, v15
	s_waitcnt vmcnt(16)
	global_store_dwordx4 v[8:9], v[18:21], off nt
	v_cvt_pk_f16_f32 v9, v20, v21
	v_cvt_pk_f16_f32 v8, v18, v19
	ds_write2_b64 v10, v[6:7], v[8:9] offset0:164 offset1:230
	v_lshl_add_u64 v[6:7], v[2:3], 0, s[24:25]
	v_lshl_add_u64 v[8:9], v[2:3], 0, s[28:29]
	s_waitcnt vmcnt(16)
	global_store_dwordx4 v[6:7], v[22:25], off nt
	v_cvt_pk_f16_f32 v7, v24, v25
	v_cvt_pk_f16_f32 v6, v22, v23
	s_waitcnt vmcnt(16)
	global_store_dwordx4 v[8:9], v[26:29], off nt
	v_cvt_pk_f16_f32 v9, v28, v29
	v_cvt_pk_f16_f32 v8, v26, v27
	v_add_u32_e32 v10, 0x2800, v78
	ds_write2_b64 v10, v[6:7], v[8:9] offset0:40 offset1:106
	v_lshl_add_u64 v[6:7], v[2:3], 0, s[26:27]
	v_lshl_add_u64 v[8:9], v[2:3], 0, s[30:31]
	s_waitcnt vmcnt(16)
	global_store_dwordx4 v[6:7], v[30:33], off nt
	v_cvt_pk_f16_f32 v7, v32, v33
	v_cvt_pk_f16_f32 v6, v30, v31
	s_waitcnt vmcnt(16)
	global_store_dwordx4 v[8:9], v[34:37], off nt
	v_cvt_pk_f16_f32 v9, v36, v37
	v_cvt_pk_f16_f32 v8, v34, v35
	ds_write2_b64 v10, v[6:7], v[8:9] offset0:172 offset1:238
	v_lshl_add_u64 v[6:7], v[2:3], 0, s[34:35]
	v_lshl_add_u64 v[8:9], v[2:3], 0, s[38:39]
	s_waitcnt vmcnt(16)
	global_store_dwordx4 v[6:7], v[38:41], off nt
	v_cvt_pk_f16_f32 v7, v40, v41
	v_cvt_pk_f16_f32 v6, v38, v39
	s_waitcnt vmcnt(16)
	global_store_dwordx4 v[8:9], v[42:45], off nt
	v_cvt_pk_f16_f32 v9, v44, v45
	v_cvt_pk_f16_f32 v8, v42, v43
	v_add_u32_e32 v10, 0x3000, v78
	ds_write2_b64 v10, v[6:7], v[8:9] offset0:48 offset1:114
	v_lshl_add_u64 v[6:7], v[2:3], 0, s[36:37]
	v_lshl_add_u64 v[8:9], v[2:3], 0, s[40:41]
	s_waitcnt vmcnt(16)
	global_store_dwordx4 v[6:7], v[46:49], off nt
	v_cvt_pk_f16_f32 v7, v48, v49
	v_cvt_pk_f16_f32 v6, v46, v47
	s_waitcnt vmcnt(16)
	global_store_dwordx4 v[8:9], v[50:53], off nt
	v_cvt_pk_f16_f32 v9, v52, v53
	v_cvt_pk_f16_f32 v8, v50, v51
	ds_write2_b64 v10, v[6:7], v[8:9] offset0:180 offset1:246
	v_lshl_add_u64 v[6:7], v[2:3], 0, s[42:43]
	v_lshl_add_u64 v[8:9], v[2:3], 0, s[46:47]
	s_waitcnt vmcnt(16)
	global_store_dwordx4 v[6:7], v[54:57], off nt
	v_cvt_pk_f16_f32 v7, v56, v57
	v_cvt_pk_f16_f32 v6, v54, v55
	s_waitcnt vmcnt(16)
	global_store_dwordx4 v[8:9], v[58:61], off nt
	v_cvt_pk_f16_f32 v9, v60, v61
	v_cvt_pk_f16_f32 v8, v58, v59
	v_add_u32_e32 v10, 0x3800, v78
	ds_write2_b64 v10, v[6:7], v[8:9] offset0:56 offset1:122
	v_lshl_add_u64 v[6:7], v[2:3], 0, s[44:45]
	v_lshl_add_u64 v[2:3], v[2:3], 0, s[48:49]
	s_waitcnt vmcnt(16)
	global_store_dwordx4 v[6:7], v[70:73], off nt
	v_cvt_pk_f16_f32 v7, v72, v73
	v_cvt_pk_f16_f32 v6, v70, v71
	s_waitcnt vmcnt(16)
	global_store_dwordx4 v[2:3], v[74:77], off nt
	v_cvt_pk_f16_f32 v3, v76, v77
	v_cvt_pk_f16_f32 v2, v74, v75
	ds_write2_b64 v10, v[6:7], v[2:3] offset0:188 offset1:254
	v_lshlrev_b32_e32 v2, 4, v5
	v_add_u32_e32 v176, v1, v2
	v_mbcnt_lo_u32_b32 v1, -1, 0
	v_mbcnt_hi_u32_b32 v14, -1, v1
	v_and_b32_e32 v6, 64, v14
	v_lshlrev_b32_e32 v10, 5, v164
	v_add_u32_e32 v15, 64, v6
	v_or_b32_e32 v6, 0x20800, v10
	s_waitcnt lgkmcnt(0)
	s_barrier
	ds_read_b128 v[94:97], v176
	ds_read_b128 v[90:93], v176 offset:32
	ds_read_b128 v[86:89], v176 offset:64
	ds_read_b128 v[82:85], v176 offset:96
	ds_read_b128 v[78:81], v176 offset:128
	ds_read_b128 v[74:77], v176 offset:160
	ds_read_b128 v[70:73], v176 offset:192
	ds_read_b128 v[66:69], v176 offset:224
	ds_read_b128 v[62:65], v176 offset:256
	ds_read_b128 v[58:61], v176 offset:288
	ds_read_b128 v[54:57], v176 offset:320
	ds_read_b128 v[50:53], v176 offset:352
	ds_read_b128 v[46:49], v176 offset:384
	ds_read_b128 v[42:45], v176 offset:416
	ds_read_b128 v[38:41], v176 offset:448
	ds_read_b128 v[34:37], v176 offset:480
	ds_read_b128 v[6:9], v6
	v_or_b32_e32 v10, 0x20810, v10
	ds_read_b128 v[10:13], v10
	v_mov_b32_e32 v3, v163
	s_waitcnt lgkmcnt(14)
	v_dot2c_f32_f16_e32 v3, v94, v94
	s_waitcnt lgkmcnt(1)
	v_max_f32_e32 v7, v7, v7
	v_max_f32_e32 v6, v6, v6
	v_max_f32_e32 v6, v6, v7
	v_max_f32_e32 v7, v9, v9
	v_max_f32_e32 v8, v8, v8
	v_dot2c_f32_f16_e32 v3, v95, v95
	v_xor_b32_e32 v1, 32, v14
	v_max_f32_e32 v7, v8, v7
	s_waitcnt lgkmcnt(0)
	v_max_f32_e32 v8, v13, v13
	v_max_f32_e32 v9, v12, v12
	v_dot2c_f32_f16_e32 v3, v96, v96
	v_cmp_lt_i32_e32 vcc, v1, v15
	v_max_f32_e32 v8, v9, v8
	v_dot2c_f32_f16_e32 v3, v97, v97
	v_cndmask_b32_e32 v1, v14, v1, vcc
	v_max3_f32 v8, v10, v11, v8
	v_dot2c_f32_f16_e32 v3, v90, v90
	v_lshlrev_b32_e32 v1, 2, v1
	v_max3_f32 v6, v6, v7, v8
	v_dot2c_f32_f16_e32 v3, v91, v91
	ds_bpermute_b32 v7, v1, v6
	v_dot2c_f32_f16_e32 v3, v92, v92
	v_dot2c_f32_f16_e32 v3, v93, v93
	v_dot2c_f32_f16_e32 v3, v86, v86
	v_dot2c_f32_f16_e32 v3, v87, v87
	v_dot2c_f32_f16_e32 v3, v88, v88
	s_waitcnt lgkmcnt(0)
	v_max_f32_e32 v7, v7, v7
	v_dot2c_f32_f16_e32 v3, v89, v89
	v_max_f32_e32 v6, v6, v7
	v_xor_b32_e32 v7, 16, v14
	v_dot2c_f32_f16_e32 v3, v82, v82
	v_cmp_lt_i32_e32 vcc, v7, v15
	v_dot2c_f32_f16_e32 v3, v83, v83
	v_dot2c_f32_f16_e32 v3, v84, v84
	v_cndmask_b32_e32 v7, v14, v7, vcc
	v_lshlrev_b32_e32 v165, 2, v7
	v_dot2c_f32_f16_e32 v3, v85, v85
	ds_bpermute_b32 v7, v165, v6
	v_dot2c_f32_f16_e32 v3, v78, v78
	v_dot2c_f32_f16_e32 v3, v79, v79
	v_dot2c_f32_f16_e32 v3, v80, v80
	v_dot2c_f32_f16_e32 v3, v81, v81
	v_dot2c_f32_f16_e32 v3, v74, v74
	s_waitcnt lgkmcnt(0)
	v_max_f32_e32 v7, v7, v7
	v_dot2c_f32_f16_e32 v3, v75, v75
	v_max_f32_e32 v6, v6, v7
	v_xor_b32_e32 v7, 8, v14
	v_dot2c_f32_f16_e32 v3, v76, v76
	v_cmp_lt_i32_e32 vcc, v7, v15
	v_dot2c_f32_f16_e32 v3, v77, v77
	v_dot2c_f32_f16_e32 v3, v70, v70
	v_cndmask_b32_e32 v7, v14, v7, vcc
	v_lshlrev_b32_e32 v172, 2, v7
	v_dot2c_f32_f16_e32 v3, v71, v71
	ds_bpermute_b32 v7, v172, v6
	v_dot2c_f32_f16_e32 v3, v72, v72
	v_dot2c_f32_f16_e32 v3, v73, v73
	v_dot2c_f32_f16_e32 v3, v66, v66
	v_dot2c_f32_f16_e32 v3, v67, v67
	v_dot2c_f32_f16_e32 v3, v68, v68
	s_waitcnt lgkmcnt(0)
	v_max_f32_e32 v7, v7, v7
	v_dot2c_f32_f16_e32 v3, v69, v69
	v_max_f32_e32 v6, v6, v7
	v_xor_b32_e32 v7, 4, v14
	v_dot2c_f32_f16_e32 v3, v62, v62
	v_cmp_lt_i32_e32 vcc, v7, v15
	v_dot2c_f32_f16_e32 v3, v63, v63
	v_dot2c_f32_f16_e32 v3, v64, v64
	v_cndmask_b32_e32 v7, v14, v7, vcc
	v_lshlrev_b32_e32 v173, 2, v7
	v_dot2c_f32_f16_e32 v3, v65, v65
	ds_bpermute_b32 v7, v173, v6
	v_dot2c_f32_f16_e32 v3, v58, v58
	v_dot2c_f32_f16_e32 v3, v59, v59
	v_dot2c_f32_f16_e32 v3, v60, v60
	v_dot2c_f32_f16_e32 v3, v61, v61
	v_dot2c_f32_f16_e32 v3, v54, v54
	s_waitcnt lgkmcnt(0)
	v_max_f32_e32 v7, v7, v7
	v_dot2c_f32_f16_e32 v3, v55, v55
	v_max_f32_e32 v6, v6, v7
	v_xor_b32_e32 v7, 2, v14
	v_dot2c_f32_f16_e32 v3, v56, v56
	v_cmp_lt_i32_e32 vcc, v7, v15
	v_dot2c_f32_f16_e32 v3, v57, v57
	v_dot2c_f32_f16_e32 v3, v50, v50
	v_cndmask_b32_e32 v7, v14, v7, vcc
	v_lshlrev_b32_e32 v174, 2, v7
	v_dot2c_f32_f16_e32 v3, v51, v51
	ds_bpermute_b32 v7, v174, v6
	v_dot2c_f32_f16_e32 v3, v52, v52
	v_dot2c_f32_f16_e32 v3, v53, v53
	v_dot2c_f32_f16_e32 v3, v46, v46
	v_dot2c_f32_f16_e32 v3, v47, v47
	v_dot2c_f32_f16_e32 v3, v48, v48
	s_waitcnt lgkmcnt(0)
	v_max_f32_e32 v7, v7, v7
	v_dot2c_f32_f16_e32 v3, v49, v49
	v_max_f32_e32 v6, v6, v7
	v_xor_b32_e32 v7, 1, v14
	v_dot2c_f32_f16_e32 v3, v42, v42
	v_cmp_lt_i32_e32 vcc, v7, v15
	v_dot2c_f32_f16_e32 v3, v43, v43
	v_dot2c_f32_f16_e32 v3, v44, v44
	v_cndmask_b32_e32 v7, v14, v7, vcc
	v_lshlrev_b32_e32 v175, 2, v7
	v_dot2c_f32_f16_e32 v3, v45, v45
	ds_bpermute_b32 v7, v175, v6
	v_dot2c_f32_f16_e32 v3, v38, v38
	v_dot2c_f32_f16_e32 v3, v39, v39
	v_dot2c_f32_f16_e32 v3, v40, v40
	v_dot2c_f32_f16_e32 v3, v41, v41
	v_dot2c_f32_f16_e32 v3, v34, v34
	s_waitcnt lgkmcnt(0)
	v_max_f32_e32 v7, v7, v7
	v_dot2c_f32_f16_e32 v3, v35, v35
	v_max_f32_e32 v6, v6, v7
	v_dot2c_f32_f16_e32 v3, v36, v36
	v_add_f32_e32 v6, v6, v6
	s_mov_b32 s41, 0xf800000
	v_dot2c_f32_f16_e32 v3, v37, v37
	v_mul_f32_e32 v7, 0x4f800000, v6
	v_cmp_gt_f32_e32 vcc, s41, v6
	s_lshl_b32 s43, s33, 7
	ds_bpermute_b32 v8, v1, v3
	v_cndmask_b32_e32 v6, v6, v7, vcc
	v_sqrt_f32_e32 v7, v6
	s_lshl_b32 s36, s33, 2
	s_lshl_b32 s45, s33, 3
	s_waitcnt lgkmcnt(0)
	v_add_f32_e32 v178, v3, v8
	v_add_u32_e32 v3, -1, v7
	v_fma_f32 v8, -v3, v7, v6
	v_cmp_ge_f32_e64 s[4:5], 0, v8
	v_add_u32_e32 v8, 1, v7
	s_add_i32 s44, s36, 0x22620
	v_cndmask_b32_e64 v3, v7, v3, s[4:5]
	v_fma_f32 v7, -v8, v7, v6
	v_cmp_lt_f32_e64 s[4:5], 0, v7
	s_add_i32 s45, s45, 0x22600
	s_add_i32 s3, s43, 0x22000
	v_cndmask_b32_e64 v3, v3, v8, s[4:5]
	v_mul_f32_e32 v7, 0x37800000, v3
	s_add_i32 s46, s98, 0x18000
	s_add_i32 s47, s36, 0x21800
	s_add_i32 s48, s36, 0x21000
	v_cndmask_b32_e32 v3, v3, v7, vcc
	v_cmp_class_f32_e32 vcc, v6, v179
	s_add_u32 s10, s14, s10
	s_addc_u32 s11, s15, s11
	v_cndmask_b32_e32 v180, v3, v6, vcc
	v_mov_b32_e32 v3, 0x22200
	v_lshl_or_b32 v183, v4, 2, v3
	v_or_b32_e32 v188, 0x20800, v2
	v_lshl_add_u64 v[2:3], s[10:11], 0, v[162:163]
	s_mov_b64 s[10:11], 0x1c00
	s_mov_b32 s24, 0x39666666
	s_mov_b32 s40, 0
	s_mov_b32 s42, 0xff800000
	v_cmp_lt_u32_e64 s[12:13], 31, v164
	v_cmp_gt_u32_e64 s[4:5], 32, v164
	v_cmp_eq_u32_e64 s[8:9], 0, v0
	v_lshl_add_u32 v186, v164, 2, s3
	v_lshl_add_u64 v[168:169], v[2:3], 0, s[10:11]
	s_mov_b32 s25, 0x39800000
	s_mov_b32 s49, 0x7149f2ca
	s_mov_b64 s[26:27], 0x2000
	s_mov_b32 s3, 0
	s_mov_b32 s22, 0
	s_mov_b32 s37, 0
	s_mov_b32 s38, 0
	s_mov_b32 s39, 0
	s_mov_b32 s23, 0
	s_barrier
	s_branch .LBB1_6
